# edge kernels: bias loads issued with the first load batch instead of behind two serial scalar-load + vmcnt(0) round trips
# speedup vs baseline: 1.0163x; 1.0063x over previous
_Z7k_edge0PK15HIP_vector_typeIfLj4EEPKDv8_DF16_S5_PKfS7_S7_PfS8_:
	s_load_dwordx4 s[8:11], s[0:1], 0x0
	s_load_dwordx2 s[4:5], s[0:1], 0x10
	s_load_dwordx2 s[6:7], s[0:1], 0x28
	v_mov_b32_e32 v31, 0
	v_lshlrev_b32_e32 v30, 4, v0
	s_load_dwordx4 s[12:15], s[0:1], 0x18
	s_waitcnt lgkmcnt(0)
	v_bfe_u32 v97, v0, 6, 1
	v_and_b32_e32 v96, 31, v0
	v_lshl_or_b32 v97, v97, 5, v96
	v_lshlrev_b32_e32 v97, 2, v97
	v_and_b32_e32 v96, 63, v0
	v_lshlrev_b32_e32 v96, 2, v96
	global_load_dword v96, v96, s[12:13]
	global_load_dword v97, v97, s[14:15]
	v_lshl_add_u64 v[2:3], s[10:11], 0, v[30:31]
	v_add_co_u32_e32 v2, vcc, 0x1000, v2
	global_load_dwordx4 v[14:17], v30, s[10:11]
	s_nop 0
	v_addc_co_u32_e32 v3, vcc, 0, v3, vcc
	global_load_dwordx4 v[22:25], v[2:3], off
	v_lshl_add_u64 v[2:3], s[4:5], 0, v[30:31]
	v_add_co_u32_e32 v2, vcc, 0x1000, v2
	s_movk_i32 s3, 0x340
	s_nop 0
	v_addc_co_u32_e32 v3, vcc, 0, v3, vcc
	global_load_dwordx4 v[36:39], v[2:3], off
	v_lshl_add_u64 v[2:3], s[6:7], 0, v[30:31]
	v_add_co_u32_e32 v4, vcc, 0x1000, v2
	global_load_dwordx4 v[48:51], v30, s[4:5]
	global_load_dwordx4 v[40:43], v30, s[6:7]
	v_addc_co_u32_e32 v5, vcc, 0, v3, vcc
	v_add_co_u32_e32 v2, vcc, 0x2000, v2
	v_or_b32_e32 v1, 0x300, v0
	s_nop 0
	v_addc_co_u32_e32 v3, vcc, 0, v3, vcc
	global_load_dwordx4 v[44:47], v[4:5], off
	global_load_dwordx4 v[18:21], v[2:3], off
	v_cmp_gt_u32_e32 vcc, s3, v0
	v_or_b32_e32 v2, 0x400, v0
	s_movk_i32 s3, 0x640
	v_cndmask_b32_e32 v1, 0, v1, vcc
	v_cmp_gt_u32_e32 vcc, s3, v2
	v_lshlrev_b32_e32 v1, 4, v1
	s_movk_i32 s3, 0x140
	v_cndmask_b32_e32 v2, 0, v2, vcc
	v_lshlrev_b32_e32 v2, 4, v2
	global_load_dwordx4 v[26:29], v1, s[6:7]
	global_load_dwordx4 v[6:9], v2, s[6:7]
	v_or_b32_e32 v1, 0x500, v0
	v_cmp_gt_u32_e32 vcc, s3, v0
	v_or_b32_e32 v2, 0x600, v0
	v_mov_b32_e32 v54, 0
	v_cndmask_b32_e32 v1, 0, v1, vcc
	v_cmp_gt_u32_e32 vcc, 64, v0
	v_lshlrev_b32_e32 v1, 4, v1
	s_nop 0
	v_cndmask_b32_e32 v2, 0, v2, vcc
	v_lshlrev_b32_e32 v32, 4, v2
	global_load_dwordx4 v[10:13], v1, s[6:7]
	global_load_dwordx4 v[2:5], v32, s[6:7]
	v_lshlrev_b32_e32 v1, 2, v0
	s_and_saveexec_b64 s[4:5], vcc
	s_cbranch_execz .LBB3_2
	s_nop 0
	s_nop 0
	s_nop 0
	s_nop 0
	s_nop 0
.LBB3_2:
	s_or_b64 exec, exec, s[4:5]
	s_movk_i32 s3, 0x80
	v_lshrrev_b32_e32 v32, 6, v0
	v_and_b32_e32 v62, 31, v0
	v_cmp_gt_u32_e64 s[4:5], s3, v0
	s_and_saveexec_b64 s[6:7], s[4:5]
	s_cbranch_execz .LBB3_4
	s_nop 0
	s_nop 0
	s_nop 0
	s_nop 0
	s_nop 0
	s_nop 0
	s_nop 0

.LBB3_7:
	s_waitcnt vmcnt(3)
	v_cvt_f16_f32_e32 v31, v97
	v_and_b32_e32 v2, 32, v0
	v_cmp_eq_u32_e32 vcc, 0, v2
	v_mov_b32_e32 v3, 0
	v_lshlrev_b32_e32 v1, 4, v0
	v_cndmask_b32_sdwa v2, v3, v31, vcc dst_sel:DWORD dst_unused:UNUSED_PAD src0_sel:DWORD src1_sel:WORD_0
	v_mov_b32_e32 v4, v3
	v_mov_b32_e32 v5, v3
	ds_write_b128 v1, v[2:5] offset:29184

.LBB3_75:
	s_waitcnt vmcnt(3)
	v_mul_f32_e32 v54, 0x3fb8aa3b, v96
	ds_write_b32 v1, v54 offset:31232
	s_or_b64 exec, exec, s[2:3]
	s_and_saveexec_b64 s[2:3], s[4:5]
	s_cbranch_execnz .LBB3_7
	s_branch .LBB3_8

	.amdhsa_kernel _Z7k_edge0PK15HIP_vector_typeIfLj4EEPKDv8_DF16_S5_PKfS7_S7_PfS8_
		.amdhsa_group_segment_fixed_size 31488
		.amdhsa_private_segment_fixed_size 0
		.amdhsa_kernarg_size 320
		.amdhsa_user_sgpr_count 2
		.amdhsa_user_sgpr_dispatch_ptr 0
		.amdhsa_user_sgpr_queue_ptr 0
		.amdhsa_user_sgpr_kernarg_segment_ptr 1
		.amdhsa_user_sgpr_dispatch_id 0
		.amdhsa_user_sgpr_kernarg_preload_length 0
		.amdhsa_user_sgpr_kernarg_preload_offset 0
		.amdhsa_user_sgpr_private_segment_size 0
		.amdhsa_uses_dynamic_stack 0
		.amdhsa_enable_private_segment 0
		.amdhsa_system_sgpr_workgroup_id_x 1
		.amdhsa_system_sgpr_workgroup_id_y 0
		.amdhsa_system_sgpr_workgroup_id_z 0
		.amdhsa_system_sgpr_workgroup_info 0
		.amdhsa_system_vgpr_workitem_id 0
		.amdhsa_next_free_vgpr 98
		.amdhsa_next_free_sgpr 96
		.amdhsa_accum_offset 100
		.amdhsa_reserve_vcc 1
		.amdhsa_float_round_mode_32 0
		.amdhsa_float_round_mode_16_64 0
		.amdhsa_float_denorm_mode_32 3
		.amdhsa_float_denorm_mode_16_64 3
		.amdhsa_dx10_clamp 1
		.amdhsa_ieee_mode 1
		.amdhsa_fp16_overflow 0
		.amdhsa_tg_split 0
		.amdhsa_exception_fp_ieee_invalid_op 0
		.amdhsa_exception_fp_denorm_src 0
		.amdhsa_exception_fp_ieee_div_zero 0
		.amdhsa_exception_fp_ieee_overflow 0
		.amdhsa_exception_fp_ieee_underflow 0
		.amdhsa_exception_fp_ieee_inexact 0
		.amdhsa_exception_int_div_zero 0
	.end_amdhsa_kernel

_Z7k_edge1PK15HIP_vector_typeIfLj4EEPKDv8_DF16_S5_PKfS7_S7_PKDv2_DF16_PfSB_:
	s_load_dwordx4 s[8:11], s[0:1], 0x0
	s_load_dwordx2 s[4:5], s[0:1], 0x10
	s_load_dwordx2 s[6:7], s[0:1], 0x28
	v_mov_b32_e32 v47, 0
	v_lshlrev_b32_e32 v46, 4, v0
	s_load_dwordx4 s[12:15], s[0:1], 0x18
	s_waitcnt lgkmcnt(0)
	v_bfe_u32 v127, v0, 6, 1
	v_and_b32_e32 v126, 31, v0
	v_lshl_or_b32 v127, v127, 5, v126
	v_lshlrev_b32_e32 v127, 2, v127
	v_and_b32_e32 v126, 63, v0
	v_lshlrev_b32_e32 v126, 2, v126
	global_load_dword v126, v126, s[12:13]
	global_load_dword v127, v127, s[14:15]
	v_lshl_add_u64 v[2:3], s[10:11], 0, v[46:47]
	v_add_co_u32_e32 v2, vcc, 0x1000, v2
	global_load_dwordx4 v[14:17], v46, s[10:11]
	s_nop 0
	v_addc_co_u32_e32 v3, vcc, 0, v3, vcc
	global_load_dwordx4 v[22:25], v[2:3], off
	v_lshl_add_u64 v[2:3], s[4:5], 0, v[46:47]
	v_add_co_u32_e32 v2, vcc, 0x1000, v2
	s_movk_i32 s3, 0x340
	s_nop 0
	v_addc_co_u32_e32 v3, vcc, 0, v3, vcc
	global_load_dwordx4 v[30:33], v[2:3], off
	v_lshl_add_u64 v[2:3], s[6:7], 0, v[46:47]
	v_add_co_u32_e32 v4, vcc, 0x1000, v2
	global_load_dwordx4 v[42:45], v46, s[4:5]
	global_load_dwordx4 v[34:37], v46, s[6:7]
	v_addc_co_u32_e32 v5, vcc, 0, v3, vcc
	v_add_co_u32_e32 v2, vcc, 0x2000, v2
	v_or_b32_e32 v1, 0x300, v0
	s_nop 0
	v_addc_co_u32_e32 v3, vcc, 0, v3, vcc
	global_load_dwordx4 v[38:41], v[4:5], off
	global_load_dwordx4 v[18:21], v[2:3], off
	v_cmp_gt_u32_e32 vcc, s3, v0
	v_or_b32_e32 v2, 0x400, v0
	s_movk_i32 s3, 0x640
	v_cndmask_b32_e32 v1, 0, v1, vcc
	v_cmp_gt_u32_e32 vcc, s3, v2
	v_lshlrev_b32_e32 v1, 4, v1
	s_movk_i32 s3, 0x140
	v_cndmask_b32_e32 v2, 0, v2, vcc
	v_lshlrev_b32_e32 v2, 4, v2
	global_load_dwordx4 v[26:29], v1, s[6:7]
	global_load_dwordx4 v[6:9], v2, s[6:7]
	v_or_b32_e32 v1, 0x500, v0
	v_cmp_gt_u32_e32 vcc, s3, v0
	v_or_b32_e32 v2, 0x600, v0
	v_mov_b32_e32 v52, 0
	v_cndmask_b32_e32 v1, 0, v1, vcc
	v_cmp_gt_u32_e32 vcc, 64, v0
	v_lshlrev_b32_e32 v1, 4, v1
	s_nop 0
	v_cndmask_b32_e32 v2, 0, v2, vcc
	v_lshlrev_b32_e32 v48, 4, v2
	global_load_dwordx4 v[10:13], v1, s[6:7]
	global_load_dwordx4 v[2:5], v48, s[6:7]
	v_lshlrev_b32_e32 v1, 2, v0
	s_and_saveexec_b64 s[4:5], vcc
	s_cbranch_execz .LBB4_2
	s_nop 0
	s_nop 0
	s_nop 0
	s_nop 0
	s_nop 0
.LBB4_2:
	s_or_b64 exec, exec, s[4:5]
	s_movk_i32 s3, 0x80
	v_lshrrev_b32_e32 v48, 6, v0
	v_and_b32_e32 v66, 31, v0
	v_cmp_gt_u32_e64 s[4:5], s3, v0
	s_and_saveexec_b64 s[6:7], s[4:5]
	s_cbranch_execz .LBB4_4
	s_nop 0
	s_nop 0
	s_nop 0
	s_nop 0
	s_nop 0
	s_nop 0
	s_nop 0

.LBB4_7:
	s_waitcnt vmcnt(3)
	v_cvt_f16_f32_e32 v47, v127
	v_and_b32_e32 v2, 32, v0
	v_cmp_eq_u32_e32 vcc, 0, v2
	v_mov_b32_e32 v3, 0
	v_lshlrev_b32_e32 v1, 4, v0
	v_cndmask_b32_sdwa v2, v3, v47, vcc dst_sel:DWORD dst_unused:UNUSED_PAD src0_sel:DWORD src1_sel:WORD_0
	v_mov_b32_e32 v4, v3
	v_mov_b32_e32 v5, v3
	ds_write_b128 v1, v[2:5] offset:29184

.LBB4_75:
	s_waitcnt vmcnt(3)
	v_mul_f32_e32 v52, 0x3fb8aa3b, v126
	ds_write_b32 v1, v52 offset:31232
	s_or_b64 exec, exec, s[2:3]
	s_and_saveexec_b64 s[2:3], s[4:5]
	s_cbranch_execnz .LBB4_7
	s_branch .LBB4_8

amdhsa.kernels:
  - .agpr_count:     0
    .args:
      - .actual_access:  read_only
        .address_space:  global
        .offset:         0
        .size:           8
        .value_kind:     global_buffer
      - .actual_access:  write_only
        .address_space:  global
        .offset:         8
        .size:           8
        .value_kind:     global_buffer
      - .offset:         16
        .size:           288
        .value_kind:     by_value
      - .actual_access:  write_only
        .address_space:  global
        .offset:         304
        .size:           8
        .value_kind:     global_buffer
      - .actual_access:  write_only
        .address_space:  global
        .offset:         312
        .size:           8
        .value_kind:     global_buffer
    .group_segment_fixed_size: 1564
    .kernarg_segment_align: 8
    .kernarg_segment_size: 320
    .language:       OpenCL C
    .language_version:
      - 2
      - 0
    .max_flat_workgroup_size: 256
    .name:           _Z8k_bcountPKiPi8PrepArgsPDF16_S3_
    .private_segment_fixed_size: 0
    .sgpr_count:     26
    .sgpr_spill_count: 0
    .symbol:         _Z8k_bcountPKiPi8PrepArgsPDF16_S3_.kd
    .uniform_work_group_size: 1
    .uses_dynamic_stack: false
    .vgpr_count:     26
    .vgpr_spill_count: 0
    .wavefront_size: 64
  - .agpr_count:     0
    .args:
      - .actual_access:  read_only
        .address_space:  global
        .offset:         0
        .size:           8
        .value_kind:     global_buffer
      - .actual_access:  read_only
        .address_space:  global
        .offset:         8
        .size:           8
        .value_kind:     global_buffer
      - .actual_access:  read_only
        .address_space:  global
        .offset:         16
        .size:           8
        .value_kind:     global_buffer
      - .actual_access:  read_only
        .address_space:  global
        .offset:         24
        .size:           8
        .value_kind:     global_buffer
      - .actual_access:  write_only
        .address_space:  global
        .offset:         32
        .size:           8
        .value_kind:     global_buffer
      - .actual_access:  write_only
        .address_space:  global
        .offset:         40
        .size:           8
        .value_kind:     global_buffer
      - .actual_access:  write_only
        .address_space:  global
        .offset:         48
        .size:           8
        .value_kind:     global_buffer
    .group_segment_fixed_size: 19228
    .kernarg_segment_align: 8
    .kernarg_segment_size: 56
    .language:       OpenCL C
    .language_version:
      - 2
      - 0
    .max_flat_workgroup_size: 512
    .name:           _Z10k_bscatterPKfPKiS2_S2_PiP15HIP_vector_typeIfLj2EEPf
    .private_segment_fixed_size: 0
    .sgpr_count:     26
    .sgpr_spill_count: 0
    .symbol:         _Z10k_bscatterPKfPKiS2_S2_PiP15HIP_vector_typeIfLj2EEPf.kd
    .uniform_work_group_size: 1
    .uses_dynamic_stack: false
    .vgpr_count:     196
    .vgpr_spill_count: 0
    .wavefront_size: 64
  - .agpr_count:     0
    .args:
      - .actual_access:  read_only
        .address_space:  global
        .offset:         0
        .size:           8
        .value_kind:     global_buffer
      - .actual_access:  read_only
        .address_space:  global
        .offset:         8
        .size:           8
        .value_kind:     global_buffer
      - .actual_access:  read_only
        .address_space:  global
        .offset:         16
        .size:           8
        .value_kind:     global_buffer
      - .actual_access:  write_only
        .address_space:  global
        .offset:         24
        .size:           8
        .value_kind:     global_buffer
      - .actual_access:  write_only
        .address_space:  global
        .offset:         32
        .size:           8
        .value_kind:     global_buffer
    .group_segment_fixed_size: 1024
    .kernarg_segment_align: 8
    .kernarg_segment_size: 40
    .language:       OpenCL C
    .language_version:
      - 2
      - 0
    .max_flat_workgroup_size: 512
    .name:           _Z7k_bsortPK15HIP_vector_typeIfLj2EEPKiS4_PS_IfLj4EEPi
    .private_segment_fixed_size: 0
    .sgpr_count:     58
    .sgpr_spill_count: 0
    .symbol:         _Z7k_bsortPK15HIP_vector_typeIfLj2EEPKiS4_PS_IfLj4EEPi.kd
    .uniform_work_group_size: 1
    .uses_dynamic_stack: false
    .vgpr_count:     71
    .vgpr_spill_count: 0
    .wavefront_size: 64
  - .agpr_count:     0
    .args:
      - .actual_access:  read_only
        .address_space:  global
        .offset:         0
        .size:           8
        .value_kind:     global_buffer
      - .actual_access:  read_only
        .address_space:  global
        .offset:         8
        .size:           8
        .value_kind:     global_buffer
      - .actual_access:  read_only
        .address_space:  global
        .offset:         16
        .size:           8
        .value_kind:     global_buffer
      - .actual_access:  read_only
        .address_space:  global
        .offset:         24
        .size:           8
        .value_kind:     global_buffer
      - .actual_access:  read_only
        .address_space:  global
        .offset:         32
        .size:           8
        .value_kind:     global_buffer
      - .actual_access:  read_only
        .address_space:  global
        .offset:         40
        .size:           8
        .value_kind:     global_buffer
      - .actual_access:  write_only
        .address_space:  global
        .offset:         48
        .size:           8
        .value_kind:     global_buffer
      - .actual_access:  write_only
        .address_space:  global
        .offset:         56
        .size:           8
        .value_kind:     global_buffer
      - .offset:         64
        .size:           4
        .value_kind:     hidden_block_count_x
      - .offset:         68
        .size:           4
        .value_kind:     hidden_block_count_y
      - .offset:         72
        .size:           4
        .value_kind:     hidden_block_count_z
      - .offset:         76
        .size:           2
        .value_kind:     hidden_group_size_x
      - .offset:         78
        .size:           2
        .value_kind:     hidden_group_size_y
      - .offset:         80
        .size:           2
        .value_kind:     hidden_group_size_z
      - .offset:         82
        .size:           2
        .value_kind:     hidden_remainder_x
      - .offset:         84
        .size:           2
        .value_kind:     hidden_remainder_y
      - .offset:         86
        .size:           2
        .value_kind:     hidden_remainder_z
      - .offset:         104
        .size:           8
        .value_kind:     hidden_global_offset_x
      - .offset:         112
        .size:           8
        .value_kind:     hidden_global_offset_y
      - .offset:         120
        .size:           8
        .value_kind:     hidden_global_offset_z
      - .offset:         128
        .size:           2
        .value_kind:     hidden_grid_dims
    .group_segment_fixed_size: 31488
    .kernarg_segment_align: 8
    .kernarg_segment_size: 320
    .language:       OpenCL C
    .language_version:
      - 2
      - 0
    .max_flat_workgroup_size: 256
    .name:           _Z7k_edge0PK15HIP_vector_typeIfLj4EEPKDv8_DF16_S5_PKfS7_S7_PfS8_
    .private_segment_fixed_size: 0
    .sgpr_count:     59
    .sgpr_spill_count: 0
    .symbol:         _Z7k_edge0PK15HIP_vector_typeIfLj4EEPKDv8_DF16_S5_PKfS7_S7_PfS8_.kd
    .uniform_work_group_size: 1
    .uses_dynamic_stack: false
    .vgpr_count:     98
    .vgpr_spill_count: 0
    .wavefront_size: 64
  - .agpr_count:     0
    .args:
      - .actual_access:  read_only
        .address_space:  global
        .offset:         0
        .size:           8
        .value_kind:     global_buffer
      - .actual_access:  read_only
        .address_space:  global
        .offset:         8
        .size:           8
        .value_kind:     global_buffer
      - .actual_access:  read_only
        .address_space:  global
        .offset:         16
        .size:           8
        .value_kind:     global_buffer
      - .actual_access:  read_only
        .address_space:  global
        .offset:         24
        .size:           8
        .value_kind:     global_buffer
      - .actual_access:  read_only
        .address_space:  global
        .offset:         32
        .size:           8
        .value_kind:     global_buffer
      - .actual_access:  read_only
        .address_space:  global
        .offset:         40
        .size:           8
        .value_kind:     global_buffer
      - .address_space:  global
        .offset:         48
        .size:           8
        .value_kind:     global_buffer
      - .actual_access:  write_only
        .address_space:  global
        .offset:         56
        .size:           8
        .value_kind:     global_buffer
      - .actual_access:  write_only
        .address_space:  global
        .offset:         64
        .size:           8
        .value_kind:     global_buffer
      - .offset:         72
        .size:           4
        .value_kind:     hidden_block_count_x
      - .offset:         76
        .size:           4
        .value_kind:     hidden_block_count_y
      - .offset:         80
        .size:           4
        .value_kind:     hidden_block_count_z
      - .offset:         84
        .size:           2
        .value_kind:     hidden_group_size_x
      - .offset:         86
        .size:           2
        .value_kind:     hidden_group_size_y
      - .offset:         88
        .size:           2
        .value_kind:     hidden_group_size_z
      - .offset:         90
        .size:           2
        .value_kind:     hidden_remainder_x
      - .offset:         92
        .size:           2
        .value_kind:     hidden_remainder_y
      - .offset:         94
        .size:           2
        .value_kind:     hidden_remainder_z
      - .offset:         112
        .size:           8
        .value_kind:     hidden_global_offset_x
      - .offset:         120
        .size:           8
        .value_kind:     hidden_global_offset_y
      - .offset:         128
        .size:           8
        .value_kind:     hidden_global_offset_z
      - .offset:         136
        .size:           2
        .value_kind:     hidden_grid_dims
    .group_segment_fixed_size: 31488
    .kernarg_segment_align: 8
    .kernarg_segment_size: 328
    .language:       OpenCL C
    .language_version:
      - 2
      - 0
    .max_flat_workgroup_size: 256
    .name:           _Z7k_edge1PK15HIP_vector_typeIfLj4EEPKDv8_DF16_S5_PKfS7_S7_PKDv2_DF16_PfSB_
    .private_segment_fixed_size: 0
    .sgpr_count:     56
    .sgpr_spill_count: 0
    .symbol:         _Z7k_edge1PK15HIP_vector_typeIfLj4EEPKDv8_DF16_S5_PKfS7_S7_PKDv2_DF16_PfSB_.kd
    .uniform_work_group_size: 1
    .uses_dynamic_stack: false
    .vgpr_count:     128
    .vgpr_spill_count: 0
    .wavefront_size: 64
  - .agpr_count:     0
    .args:
      - .actual_access:  read_only
        .address_space:  global
        .offset:         0
        .size:           8
        .value_kind:     global_buffer
      - .actual_access:  read_only
        .address_space:  global
        .offset:         8
        .size:           8
        .value_kind:     global_buffer
      - .address_space:  global
        .offset:         16
        .size:           8
        .value_kind:     global_buffer
      - .address_space:  global
        .offset:         24
        .size:           8
        .value_kind:     global_buffer
    .group_segment_fixed_size: 0
    .kernarg_segment_align: 8
    .kernarg_segment_size: 32
    .language:       OpenCL C
    .language_version:
      - 2
      - 0
    .max_flat_workgroup_size: 256
    .name:           _Z6k_poolPKfPKiPfS3_
    .private_segment_fixed_size: 0
    .sgpr_count:     20
    .sgpr_spill_count: 0
    .symbol:         _Z6k_poolPKfPKiPfS3_.kd
    .uniform_work_group_size: 1
    .uses_dynamic_stack: false
    .vgpr_count:     16
    .vgpr_spill_count: 0
    .wavefront_size: 64
  - .agpr_count:     0
    .args:
      - .actual_access:  read_only
        .address_space:  global
        .offset:         0
        .size:           8
        .value_kind:     global_buffer
      - .actual_access:  read_only
        .address_space:  global
        .offset:         8
        .size:           8
        .value_kind:     global_buffer
      - .actual_access:  read_only
        .address_space:  global
        .offset:         16
        .size:           8
        .value_kind:     global_buffer
      - .actual_access:  read_only
        .address_space:  global
        .offset:         24
        .size:           8
        .value_kind:     global_buffer
      - .actual_access:  read_only
        .address_space:  global
        .offset:         32
        .size:           8
        .value_kind:     global_buffer
      - .actual_access:  read_only
        .address_space:  global
        .offset:         40
        .size:           8
        .value_kind:     global_buffer
      - .actual_access:  write_only
        .address_space:  global
        .offset:         48
        .size:           8
        .value_kind:     global_buffer
    .group_segment_fixed_size: 20480
    .kernarg_segment_align: 8
    .kernarg_segment_size: 56
    .language:       OpenCL C
    .language_version:
      - 2
      - 0
    .max_flat_workgroup_size: 64
    .name:           _Z7k_finalPKfS0_S0_S0_S0_S0_Pf
    .private_segment_fixed_size: 0
    .sgpr_count:     42
    .sgpr_spill_count: 0
    .symbol:         _Z7k_finalPKfS0_S0_S0_S0_S0_Pf.kd
    .uniform_work_group_size: 1
    .uses_dynamic_stack: false
    .vgpr_count:     144
    .vgpr_spill_count: 0
    .wavefront_size: 64
  - .agpr_count:     0
    .args:
      - .actual_access:  read_only
        .address_space:  global
        .offset:         0
        .size:           8
        .value_kind:     global_buffer
      - .address_space:  global
        .offset:         8
        .size:           8
        .value_kind:     global_buffer
      - .address_space:  global
        .offset:         16
        .size:           8
        .value_kind:     global_buffer
      - .actual_access:  read_only
        .address_space:  global
        .offset:         24
        .size:           8
        .value_kind:     global_buffer
      - .actual_access:  read_only
        .address_space:  global
        .offset:         32
        .size:           8
        .value_kind:     global_buffer
      - .actual_access:  read_only
        .address_space:  global
        .offset:         40
        .size:           8
        .value_kind:     global_buffer
      - .actual_access:  read_only
        .address_space:  global
        .offset:         48
        .size:           8
        .value_kind:     global_buffer
      - .actual_access:  read_only
        .address_space:  global
        .offset:         56
        .size:           8
        .value_kind:     global_buffer
      - .actual_access:  read_only
        .address_space:  global
        .offset:         64
        .size:           8
        .value_kind:     global_buffer
      - .actual_access:  read_only
        .address_space:  global
        .offset:         72
        .size:           8
        .value_kind:     global_buffer
      - .actual_access:  read_only
        .address_space:  global
        .offset:         80
        .size:           8
        .value_kind:     global_buffer
      - .actual_access:  read_only
        .address_space:  global
        .offset:         88
        .size:           8
        .value_kind:     global_buffer
      - .actual_access:  read_only
        .address_space:  global
        .offset:         96
        .size:           8
        .value_kind:     global_buffer
      - .actual_access:  read_only
        .address_space:  global
        .offset:         104
        .size:           8
        .value_kind:     global_buffer
      - .actual_access:  read_only
        .address_space:  global
        .offset:         112
        .size:           8
        .value_kind:     global_buffer
    .group_segment_fixed_size: 59392
    .kernarg_segment_align: 8
    .kernarg_segment_size: 120
    .language:       OpenCL C
    .language_version:
      - 2
      - 0
    .max_flat_workgroup_size: 256
    .name:           _Z6k_nodeILi0ELi0EEvPfS0_PDv2_DF16_PKiPKfS4_S0_S0_S4_S6_PKDv8_DF16_S6_S9_S6_S9_
    .private_segment_fixed_size: 0
    .sgpr_count:     30
    .sgpr_spill_count: 0
    .symbol:         _Z6k_nodeILi0ELi0EEvPfS0_PDv2_DF16_PKiPKfS4_S0_S0_S4_S6_PKDv8_DF16_S6_S9_S6_S9_.kd
    .uniform_work_group_size: 1
    .uses_dynamic_stack: false
    .vgpr_count:     154
    .vgpr_spill_count: 0
    .wavefront_size: 64
  - .agpr_count:     0
    .args:
      - .actual_access:  read_only
        .address_space:  global
        .offset:         0
        .size:           8
        .value_kind:     global_buffer
      - .address_space:  global
        .offset:         8
        .size:           8
        .value_kind:     global_buffer
      - .address_space:  global
        .offset:         16
        .size:           8
        .value_kind:     global_buffer
      - .actual_access:  read_only
        .address_space:  global
        .offset:         24
        .size:           8
        .value_kind:     global_buffer
      - .actual_access:  read_only
        .address_space:  global
        .offset:         32
        .size:           8
        .value_kind:     global_buffer
      - .actual_access:  read_only
        .address_space:  global
        .offset:         40
        .size:           8
        .value_kind:     global_buffer
      - .actual_access:  read_only
        .address_space:  global
        .offset:         48
        .size:           8
        .value_kind:     global_buffer
      - .actual_access:  read_only
        .address_space:  global
        .offset:         56
        .size:           8
        .value_kind:     global_buffer
      - .actual_access:  read_only
        .address_space:  global
        .offset:         64
        .size:           8
        .value_kind:     global_buffer
      - .actual_access:  read_only
        .address_space:  global
        .offset:         72
        .size:           8
        .value_kind:     global_buffer
      - .actual_access:  read_only
        .address_space:  global
        .offset:         80
        .size:           8
        .value_kind:     global_buffer
      - .actual_access:  read_only
        .address_space:  global
        .offset:         88
        .size:           8
        .value_kind:     global_buffer
      - .actual_access:  read_only
        .address_space:  global
        .offset:         96
        .size:           8
        .value_kind:     global_buffer
      - .actual_access:  read_only
        .address_space:  global
        .offset:         104
        .size:           8
        .value_kind:     global_buffer
      - .actual_access:  read_only
        .address_space:  global
        .offset:         112
        .size:           8
        .value_kind:     global_buffer
    .group_segment_fixed_size: 59392
    .kernarg_segment_align: 8
    .kernarg_segment_size: 120
    .language:       OpenCL C
    .language_version:
      - 2
      - 0
    .max_flat_workgroup_size: 256
    .name:           _Z6k_nodeILi1ELi0EEvPfS0_PDv2_DF16_PKiPKfS4_S0_S0_S4_S6_PKDv8_DF16_S6_S9_S6_S9_
    .private_segment_fixed_size: 0
    .sgpr_count:     30
    .sgpr_spill_count: 0
    .symbol:         _Z6k_nodeILi1ELi0EEvPfS0_PDv2_DF16_PKiPKfS4_S0_S0_S4_S6_PKDv8_DF16_S6_S9_S6_S9_.kd
    .uniform_work_group_size: 1
    .uses_dynamic_stack: false
    .vgpr_count:     220
    .vgpr_spill_count: 0
    .wavefront_size: 64
  - .agpr_count:     0
    .args:
      - .actual_access:  read_only
        .address_space:  global
        .offset:         0
        .size:           8
        .value_kind:     global_buffer
      - .actual_access:  read_only
        .address_space:  global
        .offset:         8
        .size:           8
        .value_kind:     global_buffer
      - .address_space:  global
        .offset:         16
        .size:           8
        .value_kind:     global_buffer
      - .actual_access:  read_only
        .address_space:  global
        .offset:         24
        .size:           8
        .value_kind:     global_buffer
      - .actual_access:  read_only
        .address_space:  global
        .offset:         32
        .size:           8
        .value_kind:     global_buffer
      - .actual_access:  read_only
        .address_space:  global
        .offset:         40
        .size:           8
        .value_kind:     global_buffer
      - .address_space:  global
        .offset:         48
        .size:           8
        .value_kind:     global_buffer
      - .address_space:  global
        .offset:         56
        .size:           8
        .value_kind:     global_buffer
      - .actual_access:  read_only
        .address_space:  global
        .offset:         64
        .size:           8
        .value_kind:     global_buffer
      - .actual_access:  read_only
        .address_space:  global
        .offset:         72
        .size:           8
        .value_kind:     global_buffer
      - .actual_access:  read_only
        .address_space:  global
        .offset:         80
        .size:           8
        .value_kind:     global_buffer
      - .actual_access:  read_only
        .address_space:  global
        .offset:         88
        .size:           8
        .value_kind:     global_buffer
      - .actual_access:  read_only
        .address_space:  global
        .offset:         96
        .size:           8
        .value_kind:     global_buffer
      - .actual_access:  read_only
        .address_space:  global
        .offset:         104
        .size:           8
        .value_kind:     global_buffer
      - .actual_access:  read_only
        .address_space:  global
        .offset:         112
        .size:           8
        .value_kind:     global_buffer
    .group_segment_fixed_size: 59392
    .kernarg_segment_align: 8
    .kernarg_segment_size: 120
    .language:       OpenCL C
    .language_version:
      - 2
      - 0
    .max_flat_workgroup_size: 256
    .name:           _Z6k_nodeILi1ELi1EEvPfS0_PDv2_DF16_PKiPKfS4_S0_S0_S4_S6_PKDv8_DF16_S6_S9_S6_S9_
    .private_segment_fixed_size: 0
    .sgpr_count:     30
    .sgpr_spill_count: 0
    .symbol:         _Z6k_nodeILi1ELi1EEvPfS0_PDv2_DF16_PKiPKfS4_S0_S0_S4_S6_PKDv8_DF16_S6_S9_S6_S9_.kd
    .uniform_work_group_size: 1
    .uses_dynamic_stack: false
    .vgpr_count:     220
    .vgpr_spill_count: 0
    .wavefront_size: 64
